# plus route-phase prefix LDS reads batched, MoE1/MoE2 accumulator zeroing removed (first K-iteration peeled with C=0)
# speedup vs baseline: 1.0065x; 1.0065x over previous
.LBB0_1666:
	ds_read2_b32 v[6:7], v3 offset1:32
	ds_read2_b32 v[8:9], v3 offset0:64 offset1:96
	ds_read2_b32 v[10:11], v3 offset0:128 offset1:160
	ds_read2_b32 v[12:13], v3 offset0:192 offset1:224
	s_cmp_eq_u32 s2, s8
	s_cselect_b64 vcc, -1, 0
	s_add_i32 s9, s8, 1
	v_cndmask_b32_e32 v5, v5, v4, vcc
	s_waitcnt lgkmcnt(0)
	v_add_u32_e32 v4, v6, v4
	s_cmp_eq_u32 s9, s2
	s_cselect_b64 vcc, -1, 0
	s_add_i32 s9, s8, 2
	v_cndmask_b32_e32 v5, v5, v4, vcc
	v_add_u32_e32 v4, v7, v4
	s_cmp_eq_u32 s9, s2
	s_cselect_b64 vcc, -1, 0
	s_add_i32 s9, s8, 3
	v_cndmask_b32_e32 v5, v5, v4, vcc
	v_add_u32_e32 v4, v8, v4
	s_cmp_eq_u32 s9, s2
	s_cselect_b64 vcc, -1, 0
	s_add_i32 s9, s8, 4
	v_cndmask_b32_e32 v5, v5, v4, vcc
	v_add_u32_e32 v4, v9, v4
	s_cmp_eq_u32 s9, s2
	s_cselect_b64 vcc, -1, 0
	s_add_i32 s9, s8, 5
	v_cndmask_b32_e32 v5, v5, v4, vcc
	v_add_u32_e32 v4, v10, v4
	s_cmp_eq_u32 s9, s2
	s_cselect_b64 vcc, -1, 0
	s_add_i32 s9, s8, 6
	v_cndmask_b32_e32 v5, v5, v4, vcc
	v_add_u32_e32 v4, v11, v4
	s_cmp_eq_u32 s9, s2
	s_cselect_b64 vcc, -1, 0
	s_add_i32 s9, s8, 7
	v_cndmask_b32_e32 v5, v5, v4, vcc
	v_add_u32_e32 v4, v12, v4
	s_cmp_eq_u32 s9, s2
	s_cselect_b64 vcc, -1, 0
	s_add_i32 s9, s8, 8
	v_cndmask_b32_e32 v5, v5, v4, vcc
	v_add_u32_e32 v4, v13, v4
	s_add_i32 s8, s8, 8
	v_add_u32_e32 v3, 0x400, v3
	s_cmp_eq_u32 s8, s76
	s_cbranch_scc0 .LBB0_1666
	s_branch .LBB0_1685

.LBB0_1787:
	s_lshl_b32 s20, s63, 10
	s_add_i32 s20, s20, 0
	s_add_i32 s20, s20, 0x20800
	s_add_u32 s68, s18, 0x100
	v_lshl_add_u32 v209, v170, 2, s20
	v_lshl_add_u32 v210, v171, 2, s20
	s_addc_u32 s69, s19, 0
	s_mov_b32 s70, -2
	s_mov_b64 s[18:19], s[10:11]
	ds_read_b32 v0, v209 offset:512
	ds_read_b32 v166, v210 offset:512
	ds_read_b128 v[22:25], v186
	ds_read_b128 v[18:21], v175
	ds_read_b128 v[26:29], v176
	ds_read_b128 v[30:33], v187
	ds_read_b128 v[6:9], v188
	ds_read_b128 v[2:5], v177
	ds_read_b128 v[10:13], v178
	ds_read_b128 v[14:17], v189
	s_add_u32 s22, s18, 0x80
	s_addc_u32 s23, s19, 0
	s_cmp_eq_u32 s70, 4
	s_cselect_b64 s[24:25], -1, 0
	s_and_b64 s[20:21], s[24:25], exec
	s_cselect_b32 s21, s5, s23
	s_cselect_b32 s20, s4, s22
	s_cselect_b32 s22, s14, s68
	s_cselect_b32 s23, s15, s69
	s_and_b64 s[24:25], s[16:17], s[24:25]
	v_add_u32_e32 v211, 0, v174
	s_waitcnt lgkmcnt(0)
	v_lshl_or_b32 v0, v0, 10, v173
	s_add_i32 m0, s31, 0xc000
	ds_read_b128 v[230:233], v211
	ds_read_b128 v[238:241], v211 offset:2048
	ds_read_b128 v[234:237], v190
	ds_read_b128 v[242:245], v190 offset:2048
	ds_read_b128 v[246:249], v211 offset:4096
	ds_read_b128 v[222:225], v211 offset:6144
	ds_read_b128 v[250:253], v190 offset:4096
	ds_read_b128 v[226:229], v190 offset:6144
	global_load_lds_dwordx4 v0, s[18:19]
	v_lshl_or_b32 v0, v166, 10, v173
	s_add_i32 m0, s31, 0xe000
	s_nop 0
	global_load_lds_dwordx4 v0, s[18:19]
	s_waitcnt vmcnt(8)
	s_waitcnt lgkmcnt(0)
	s_barrier
	s_setprio 1
	s_waitcnt lgkmcnt(0)
	v_mfma_scale_f32_16x16x128_f8f6f4 v[158:161], v[18:25], v[230:237], 0, v172, v172 op_sel_hi:[0,0,0]
	v_mfma_scale_f32_16x16x128_f8f6f4 v[150:153], v[26:33], v[230:237], 0, v172, v172 op_sel_hi:[0,0,0]
	v_mfma_scale_f32_16x16x128_f8f6f4 v[142:145], v[18:25], v[238:245], 0, v172, v172 op_sel_hi:[0,0,0]
	v_mfma_scale_f32_16x16x128_f8f6f4 v[134:137], v[26:33], v[238:245], 0, v172, v172 op_sel_hi:[0,0,0]
	v_mfma_scale_f32_16x16x128_f8f6f4 v[126:129], v[18:25], v[246:253], 0, v172, v172 op_sel_hi:[0,0,0]
	v_mfma_scale_f32_16x16x128_f8f6f4 v[118:121], v[26:33], v[246:253], 0, v172, v172 op_sel_hi:[0,0,0]
	v_mfma_scale_f32_16x16x128_f8f6f4 v[110:113], v[18:25], v[222:229], 0, v172, v172 op_sel_hi:[0,0,0]
	v_mfma_scale_f32_16x16x128_f8f6f4 v[102:105], v[26:33], v[222:229], 0, v172, v172 op_sel_hi:[0,0,0]
	s_setprio 0
	s_setprio 1
	s_and_b64 s[24:25], s[24:25], exec
	v_mfma_scale_f32_16x16x128_f8f6f4 v[154:157], v[2:9], v[230:237], 0, v172, v172 op_sel_hi:[0,0,0]
	v_mfma_scale_f32_16x16x128_f8f6f4 v[146:149], v[10:17], v[230:237], 0, v172, v172 op_sel_hi:[0,0,0]
	v_mfma_scale_f32_16x16x128_f8f6f4 v[138:141], v[2:9], v[238:245], 0, v172, v172 op_sel_hi:[0,0,0]
	v_mfma_scale_f32_16x16x128_f8f6f4 v[130:133], v[10:17], v[238:245], 0, v172, v172 op_sel_hi:[0,0,0]
	v_mfma_scale_f32_16x16x128_f8f6f4 v[122:125], v[2:9], v[246:253], 0, v172, v172 op_sel_hi:[0,0,0]
	v_mfma_scale_f32_16x16x128_f8f6f4 v[114:117], v[10:17], v[246:253], 0, v172, v172 op_sel_hi:[0,0,0]
	v_mfma_scale_f32_16x16x128_f8f6f4 v[106:109], v[2:9], v[222:229], 0, v172, v172 op_sel_hi:[0,0,0]
	v_mfma_scale_f32_16x16x128_f8f6f4 v[98:101], v[10:17], v[222:229], 0, v172, v172 op_sel_hi:[0,0,0]
	s_cselect_b32 s24, s53, s63
	s_setprio 0
	s_barrier
	s_lshl_b32 s24, s24, 10
	s_add_i32 s24, s24, 0
	s_add_i32 s24, s24, 0x20800
	v_lshl_add_u32 v0, v170, 2, s24
	v_lshl_add_u32 v214, v171, 2, s24
	ds_read_b32 v166, v0
	ds_read_b32 v167, v214
	ds_read_b128 v[226:229], v191
	s_mov_b32 m0, s34
	s_add_u32 s24, s22, 0x20000
	s_waitcnt lgkmcnt(0)
	v_lshl_or_b32 v215, v166, 10, v173
	v_lshl_or_b32 v216, v167, 10, v173
	v_lshl_add_u64 v[166:167], s[22:23], 0, v[164:165]
	ds_read_b128 v[222:225], v211 offset:16384
	ds_read_b128 v[230:233], v211 offset:18432
	ds_read_b128 v[234:237], v192
	ds_read_b128 v[242:245], v193
	ds_read_b128 v[238:241], v211 offset:20480
	ds_read_b128 v[246:249], v211 offset:22528
	ds_read_b128 v[250:253], v194
	global_load_lds_dwordx4 v[166:167], off
	v_lshl_add_u64 v[168:169], s[22:23], 0, v[162:163]
	s_mov_b32 m0, s35
	s_addc_u32 s25, s23, 0
	global_load_lds_dwordx4 v[168:169], off
	v_lshl_add_u64 v[212:213], s[24:25], 0, v[164:165]
	s_mov_b32 m0, s36
	s_nop 0
	global_load_lds_dwordx4 v[212:213], off
	v_lshl_add_u64 v[212:213], s[24:25], 0, v[162:163]
	s_mov_b32 m0, s37
	s_nop 0
	global_load_lds_dwordx4 v[212:213], off
	s_mov_b32 m0, s31
	s_nop 0
	global_load_lds_dwordx4 v215, s[20:21]
	s_mov_b32 m0, s40
	s_nop 0
	global_load_lds_dwordx4 v216, s[20:21]
	s_waitcnt vmcnt(8)
	s_waitcnt lgkmcnt(0)
	s_barrier
	s_setprio 1
	s_waitcnt lgkmcnt(0)
	v_mfma_scale_f32_16x16x128_f8f6f4 v[94:97], v[18:25], v[222:229], 0, v172, v172 op_sel_hi:[0,0,0]
	v_mfma_scale_f32_16x16x128_f8f6f4 v[86:89], v[26:33], v[222:229], 0, v172, v172 op_sel_hi:[0,0,0]
	v_mfma_scale_f32_16x16x128_f8f6f4 v[78:81], v[18:25], v[230:237], 0, v172, v172 op_sel_hi:[0,0,0]
	v_mfma_scale_f32_16x16x128_f8f6f4 v[70:73], v[26:33], v[230:237], 0, v172, v172 op_sel_hi:[0,0,0]
	v_mfma_scale_f32_16x16x128_f8f6f4 v[62:65], v[18:25], v[238:245], 0, v172, v172 op_sel_hi:[0,0,0]
	v_mfma_scale_f32_16x16x128_f8f6f4 v[54:57], v[26:33], v[238:245], 0, v172, v172 op_sel_hi:[0,0,0]
	v_mfma_scale_f32_16x16x128_f8f6f4 v[46:49], v[18:25], v[246:253], 0, v172, v172 op_sel_hi:[0,0,0]
	v_mfma_scale_f32_16x16x128_f8f6f4 v[38:41], v[26:33], v[246:253], 0, v172, v172 op_sel_hi:[0,0,0]
	s_setprio 0
	s_setprio 1
	v_mfma_scale_f32_16x16x128_f8f6f4 v[90:93], v[2:9], v[222:229], 0, v172, v172 op_sel_hi:[0,0,0]
	v_mfma_scale_f32_16x16x128_f8f6f4 v[82:85], v[10:17], v[222:229], 0, v172, v172 op_sel_hi:[0,0,0]
	v_mfma_scale_f32_16x16x128_f8f6f4 v[74:77], v[2:9], v[230:237], 0, v172, v172 op_sel_hi:[0,0,0]
	v_mfma_scale_f32_16x16x128_f8f6f4 v[66:69], v[10:17], v[230:237], 0, v172, v172 op_sel_hi:[0,0,0]
	v_mfma_scale_f32_16x16x128_f8f6f4 v[58:61], v[2:9], v[238:245], 0, v172, v172 op_sel_hi:[0,0,0]
	v_mfma_scale_f32_16x16x128_f8f6f4 v[50:53], v[10:17], v[238:245], 0, v172, v172 op_sel_hi:[0,0,0]
	v_mfma_scale_f32_16x16x128_f8f6f4 v[42:45], v[2:9], v[246:253], 0, v172, v172 op_sel_hi:[0,0,0]
	v_mfma_scale_f32_16x16x128_f8f6f4 v[34:37], v[10:17], v[246:253], 0, v172, v172 op_sel_hi:[0,0,0]
	s_setprio 0
	s_barrier
	ds_read_b32 v2, v0 offset:512
	s_waitcnt lgkmcnt(0)
	v_lshl_or_b32 v212, v2, 10, v173
	ds_read_b32 v2, v214 offset:512
	s_waitcnt lgkmcnt(0)
	v_lshl_or_b32 v213, v2, 10, v173
	ds_read_b128 v[2:5], v179
	ds_read_b128 v[6:9], v195
	ds_read_b128 v[18:21], v180
	ds_read_b128 v[22:25], v196
	ds_read_b128 v[10:13], v181
	ds_read_b128 v[14:17], v197
	ds_read_b128 v[26:29], v182
	ds_read_b128 v[30:33], v198
	s_mov_b32 m0, s41
	ds_read_b128 v[222:225], v211 offset:32768
	ds_read_b128 v[230:233], v211 offset:34816
	ds_read_b128 v[226:229], v199
	ds_read_b128 v[234:237], v200
	ds_read_b128 v[238:241], v211 offset:36864
	ds_read_b128 v[246:249], v211 offset:38912
	ds_read_b128 v[242:245], v201
	ds_read_b128 v[250:253], v202
	global_load_lds_dwordx4 v212, s[20:21]
	s_mov_b32 m0, s42
	s_nop 0
	global_load_lds_dwordx4 v213, s[20:21]
	s_waitcnt vmcnt(8)
	s_waitcnt lgkmcnt(0)
	s_barrier
	s_setprio 1
	s_waitcnt lgkmcnt(0)
	v_mfma_scale_f32_16x16x128_f8f6f4 v[158:161], v[2:9], v[222:229], v[158:161], v172, v172 op_sel_hi:[0,0,0]
	v_mfma_scale_f32_16x16x128_f8f6f4 v[150:153], v[18:25], v[222:229], v[150:153], v172, v172 op_sel_hi:[0,0,0]
	v_mfma_scale_f32_16x16x128_f8f6f4 v[142:145], v[2:9], v[230:237], v[142:145], v172, v172 op_sel_hi:[0,0,0]
	v_mfma_scale_f32_16x16x128_f8f6f4 v[134:137], v[18:25], v[230:237], v[134:137], v172, v172 op_sel_hi:[0,0,0]
	v_mfma_scale_f32_16x16x128_f8f6f4 v[126:129], v[2:9], v[238:245], v[126:129], v172, v172 op_sel_hi:[0,0,0]
	v_mfma_scale_f32_16x16x128_f8f6f4 v[118:121], v[18:25], v[238:245], v[118:121], v172, v172 op_sel_hi:[0,0,0]
	v_mfma_scale_f32_16x16x128_f8f6f4 v[110:113], v[2:9], v[246:253], v[110:113], v172, v172 op_sel_hi:[0,0,0]
	v_mfma_scale_f32_16x16x128_f8f6f4 v[102:105], v[18:25], v[246:253], v[102:105], v172, v172 op_sel_hi:[0,0,0]
	s_setprio 0
	s_setprio 1
	v_mfma_scale_f32_16x16x128_f8f6f4 v[154:157], v[10:17], v[222:229], v[154:157], v172, v172 op_sel_hi:[0,0,0]
	v_mfma_scale_f32_16x16x128_f8f6f4 v[146:149], v[26:33], v[222:229], v[146:149], v172, v172 op_sel_hi:[0,0,0]
	v_mfma_scale_f32_16x16x128_f8f6f4 v[138:141], v[10:17], v[230:237], v[138:141], v172, v172 op_sel_hi:[0,0,0]
	v_mfma_scale_f32_16x16x128_f8f6f4 v[130:133], v[26:33], v[230:237], v[130:133], v172, v172 op_sel_hi:[0,0,0]
	v_mfma_scale_f32_16x16x128_f8f6f4 v[122:125], v[10:17], v[238:245], v[122:125], v172, v172 op_sel_hi:[0,0,0]
	v_mfma_scale_f32_16x16x128_f8f6f4 v[114:117], v[26:33], v[238:245], v[114:117], v172, v172 op_sel_hi:[0,0,0]
	v_mfma_scale_f32_16x16x128_f8f6f4 v[106:109], v[10:17], v[246:253], v[106:109], v172, v172 op_sel_hi:[0,0,0]
	v_mfma_scale_f32_16x16x128_f8f6f4 v[98:101], v[26:33], v[246:253], v[98:101], v172, v172 op_sel_hi:[0,0,0]
	s_setprio 0
	s_barrier
	s_mov_b32 m0, s43
	ds_read_b32 v0, v0
	ds_read_b32 v212, v214
	ds_read_b128 v[226:229], v203
	v_lshl_add_u64 v[166:167], v[166:167], 0, s[78:79]
	s_add_u32 s22, s22, 0x20080
	ds_read_b128 v[222:225], v211 offset:49152
	ds_read_b128 v[230:233], v211 offset:51200
	ds_read_b128 v[234:237], v206
	ds_read_b128 v[242:245], v207
	ds_read_b128 v[238:241], v211 offset:53248
	ds_read_b128 v[246:249], v211 offset:55296
	ds_read_b128 v[250:253], v208
	global_load_lds_dwordx4 v[166:167], off
	v_lshl_add_u64 v[166:167], v[168:169], 0, s[78:79]
	s_mov_b32 m0, s44
	s_addc_u32 s23, s23, 0
	global_load_lds_dwordx4 v[166:167], off
	v_lshl_add_u64 v[166:167], s[22:23], 0, v[164:165]
	s_mov_b32 m0, s51
	s_waitcnt lgkmcnt(0)
	v_lshl_or_b32 v0, v0, 10, v173
	global_load_lds_dwordx4 v[166:167], off
	v_lshl_add_u64 v[166:167], s[22:23], 0, v[162:163]
	s_mov_b32 m0, s52
	v_lshl_or_b32 v212, v212, 10, v173
	global_load_lds_dwordx4 v[166:167], off
	v_lshl_add_u64 v[166:167], s[20:21], 0, v[0:1]
	v_lshl_add_u64 v[166:167], v[166:167], 0, s[78:79]
	s_mov_b32 m0, s45
	v_mov_b32_e32 v213, v1
	global_load_lds_dwordx4 v[166:167], off
	v_lshl_add_u64 v[166:167], s[20:21], 0, v[212:213]
	v_lshl_add_u64 v[166:167], v[166:167], 0, s[78:79]
	s_mov_b32 m0, s48
	s_nop 0
	global_load_lds_dwordx4 v[166:167], off
	s_waitcnt vmcnt(8)
	s_waitcnt lgkmcnt(0)
	s_barrier
	s_setprio 1
	v_mfma_scale_f32_16x16x128_f8f6f4 v[94:97], v[2:9], v[222:229], v[94:97], v172, v172 op_sel_hi:[0,0,0]
	v_mfma_scale_f32_16x16x128_f8f6f4 v[86:89], v[18:25], v[222:229], v[86:89], v172, v172 op_sel_hi:[0,0,0]
	v_mfma_scale_f32_16x16x128_f8f6f4 v[78:81], v[2:9], v[230:237], v[78:81], v172, v172 op_sel_hi:[0,0,0]
	v_mfma_scale_f32_16x16x128_f8f6f4 v[70:73], v[18:25], v[230:237], v[70:73], v172, v172 op_sel_hi:[0,0,0]
	v_mfma_scale_f32_16x16x128_f8f6f4 v[62:65], v[2:9], v[238:245], v[62:65], v172, v172 op_sel_hi:[0,0,0]
	v_mfma_scale_f32_16x16x128_f8f6f4 v[54:57], v[18:25], v[238:245], v[54:57], v172, v172 op_sel_hi:[0,0,0]
	v_mfma_scale_f32_16x16x128_f8f6f4 v[46:49], v[2:9], v[246:253], v[46:49], v172, v172 op_sel_hi:[0,0,0]
	v_mfma_scale_f32_16x16x128_f8f6f4 v[38:41], v[18:25], v[246:253], v[38:41], v172, v172 op_sel_hi:[0,0,0]
	s_setprio 0
	s_setprio 1
	v_mfma_scale_f32_16x16x128_f8f6f4 v[90:93], v[10:17], v[222:229], v[90:93], v172, v172 op_sel_hi:[0,0,0]
	v_mfma_scale_f32_16x16x128_f8f6f4 v[82:85], v[26:33], v[222:229], v[82:85], v172, v172 op_sel_hi:[0,0,0]
	v_mfma_scale_f32_16x16x128_f8f6f4 v[74:77], v[10:17], v[230:237], v[74:77], v172, v172 op_sel_hi:[0,0,0]
	v_mfma_scale_f32_16x16x128_f8f6f4 v[66:69], v[26:33], v[230:237], v[66:69], v172, v172 op_sel_hi:[0,0,0]
	v_mfma_scale_f32_16x16x128_f8f6f4 v[58:61], v[10:17], v[238:245], v[58:61], v172, v172 op_sel_hi:[0,0,0]
	v_mfma_scale_f32_16x16x128_f8f6f4 v[50:53], v[26:33], v[238:245], v[50:53], v172, v172 op_sel_hi:[0,0,0]
	v_mfma_scale_f32_16x16x128_f8f6f4 v[42:45], v[10:17], v[246:253], v[42:45], v172, v172 op_sel_hi:[0,0,0]
	v_mfma_scale_f32_16x16x128_f8f6f4 v[34:37], v[26:33], v[246:253], v[34:37], v172, v172 op_sel_hi:[0,0,0]
	s_setprio 0
	s_barrier
	s_add_i32 s70, s70, 2
	s_add_u32 s18, s18, 0x100
	s_addc_u32 s19, s19, 0
	s_add_u32 s68, s68, 0x100
	s_addc_u32 s69, s69, 0
	s_cmp_gt_u32 s70, 5

.LBB0_1871:
	s_add_u32 s13, s20, 0x100
	s_addc_u32 s49, s21, 0
	s_mov_b32 s68, -2
	ds_read_b128 v[18:21], v182
	ds_read_b128 v[26:29], v183
	ds_read_b128 v[22:25], v193
	ds_read_b128 v[30:33], v194
	ds_read_b128 v[2:5], v184
	ds_read_b128 v[10:13], v185
	ds_read_b128 v[6:9], v195
	ds_read_b128 v[14:17], v196
	s_add_u32 s20, s18, 0x100
	s_addc_u32 s21, s19, 0
	s_cmp_eq_u32 s68, 4
	s_cselect_b32 s25, s15, s21
	s_cselect_b32 s24, s14, s20
	s_cselect_b32 s23, s17, s49
	s_cselect_b32 s22, s16, s13
	v_add_u32_e32 v234, 0, v181
	v_lshl_add_u64 v[212:213], s[18:19], 0, v[168:169]
	s_add_i32 m0, s36, 0xc000
	ds_read_b128 v[172:175], v234
	ds_read_b128 v[222:225], v234 offset:2048
	ds_read_b128 v[176:179], v197
	ds_read_b128 v[226:229], v197 offset:2048
	ds_read_b128 v[236:239], v234 offset:4096
	ds_read_b128 v[244:247], v234 offset:6144
	ds_read_b128 v[240:243], v197 offset:4096
	ds_read_b128 v[248:251], v197 offset:6144
	global_load_lds_dwordx4 v[212:213], off
	v_lshl_add_u64 v[212:213], s[18:19], 0, v[170:171]
	s_add_i32 m0, s36, 0xe000
	s_nop 0
	global_load_lds_dwordx4 v[212:213], off
	s_waitcnt vmcnt(8)
	s_waitcnt lgkmcnt(0)
	s_barrier
	s_setprio 1
	s_waitcnt lgkmcnt(0)
	v_mfma_scale_f32_16x16x128_f8f6f4 v[158:161], v[18:25], v[172:179], 0, v180, v180 op_sel_hi:[0,0,0]
	v_mfma_scale_f32_16x16x128_f8f6f4 v[154:157], v[26:33], v[172:179], 0, v180, v180 op_sel_hi:[0,0,0]
	v_mfma_scale_f32_16x16x128_f8f6f4 v[150:153], v[18:25], v[222:229], 0, v180, v180 op_sel_hi:[0,0,0]
	v_mfma_scale_f32_16x16x128_f8f6f4 v[146:149], v[26:33], v[222:229], 0, v180, v180 op_sel_hi:[0,0,0]
	v_mfma_scale_f32_16x16x128_f8f6f4 v[126:129], v[18:25], v[236:243], 0, v180, v180 op_sel_hi:[0,0,0]
	v_mfma_scale_f32_16x16x128_f8f6f4 v[122:125], v[26:33], v[236:243], 0, v180, v180 op_sel_hi:[0,0,0]
	v_mfma_scale_f32_16x16x128_f8f6f4 v[118:121], v[18:25], v[244:251], 0, v180, v180 op_sel_hi:[0,0,0]
	v_mfma_scale_f32_16x16x128_f8f6f4 v[114:117], v[26:33], v[244:251], 0, v180, v180 op_sel_hi:[0,0,0]
	s_setprio 0
	s_setprio 1
	v_mfma_scale_f32_16x16x128_f8f6f4 v[142:145], v[2:9], v[172:179], 0, v180, v180 op_sel_hi:[0,0,0]
	v_mfma_scale_f32_16x16x128_f8f6f4 v[138:141], v[10:17], v[172:179], 0, v180, v180 op_sel_hi:[0,0,0]
	v_mfma_scale_f32_16x16x128_f8f6f4 v[134:137], v[2:9], v[222:229], 0, v180, v180 op_sel_hi:[0,0,0]
	v_mfma_scale_f32_16x16x128_f8f6f4 v[130:133], v[10:17], v[222:229], 0, v180, v180 op_sel_hi:[0,0,0]
	v_mfma_scale_f32_16x16x128_f8f6f4 v[110:113], v[2:9], v[236:243], 0, v180, v180 op_sel_hi:[0,0,0]
	v_mfma_scale_f32_16x16x128_f8f6f4 v[106:109], v[10:17], v[236:243], 0, v180, v180 op_sel_hi:[0,0,0]
	v_mfma_scale_f32_16x16x128_f8f6f4 v[102:105], v[2:9], v[244:251], 0, v180, v180 op_sel_hi:[0,0,0]
	v_mfma_scale_f32_16x16x128_f8f6f4 v[98:101], v[10:17], v[244:251], 0, v180, v180 op_sel_hi:[0,0,0]
	s_setprio 0
	s_barrier
	s_mov_b32 m0, s37
	v_lshl_add_u64 v[172:173], s[22:23], 0, v[0:1]
	s_add_u32 s18, s22, 0x20000
	ds_read_b128 v[222:225], v234 offset:16384
	ds_read_b128 v[236:239], v234 offset:18432
	ds_read_b128 v[226:229], v198
	ds_read_b128 v[240:243], v199
	ds_read_b128 v[244:247], v234 offset:20480
	ds_read_b128 v[212:215], v234 offset:22528
	ds_read_b128 v[248:251], v200
	ds_read_b128 v[216:219], v201
	global_load_lds_dwordx4 v[172:173], off
	v_lshl_add_u64 v[174:175], s[22:23], 0, v[162:163]
	s_mov_b32 m0, s40
	s_addc_u32 s19, s23, 0
	global_load_lds_dwordx4 v[174:175], off
	v_lshl_add_u64 v[176:177], s[18:19], 0, v[0:1]
	s_mov_b32 m0, s41
	v_lshl_add_u64 v[178:179], s[24:25], 0, v[166:167]
	global_load_lds_dwordx4 v[176:177], off
	v_lshl_add_u64 v[176:177], s[18:19], 0, v[162:163]
	s_mov_b32 m0, s42
	s_nop 0
	global_load_lds_dwordx4 v[176:177], off
	v_lshl_add_u64 v[176:177], s[24:25], 0, v[164:165]
	s_mov_b32 m0, s36
	s_nop 0
	global_load_lds_dwordx4 v[176:177], off
	s_mov_b32 m0, s43
	s_nop 0
	global_load_lds_dwordx4 v[178:179], off
	s_waitcnt vmcnt(8)
	s_waitcnt lgkmcnt(0)
	s_barrier
	s_setprio 1
	s_waitcnt lgkmcnt(0)
	v_mfma_scale_f32_16x16x128_f8f6f4 v[94:97], v[18:25], v[222:229], 0, v180, v180 op_sel_hi:[0,0,0]
	v_mfma_scale_f32_16x16x128_f8f6f4 v[90:93], v[26:33], v[222:229], 0, v180, v180 op_sel_hi:[0,0,0]
	v_mfma_scale_f32_16x16x128_f8f6f4 v[86:89], v[18:25], v[236:243], 0, v180, v180 op_sel_hi:[0,0,0]
	v_mfma_scale_f32_16x16x128_f8f6f4 v[82:85], v[26:33], v[236:243], 0, v180, v180 op_sel_hi:[0,0,0]
	v_mfma_scale_f32_16x16x128_f8f6f4 v[62:65], v[18:25], v[244:251], 0, v180, v180 op_sel_hi:[0,0,0]
	v_mfma_scale_f32_16x16x128_f8f6f4 v[58:61], v[26:33], v[244:251], 0, v180, v180 op_sel_hi:[0,0,0]
	v_mfma_scale_f32_16x16x128_f8f6f4 v[54:57], v[18:25], v[212:219], 0, v180, v180 op_sel_hi:[0,0,0]
	v_mfma_scale_f32_16x16x128_f8f6f4 v[50:53], v[26:33], v[212:219], 0, v180, v180 op_sel_hi:[0,0,0]
	s_setprio 0
	s_setprio 1
	v_mfma_scale_f32_16x16x128_f8f6f4 v[78:81], v[2:9], v[222:229], 0, v180, v180 op_sel_hi:[0,0,0]
	v_mfma_scale_f32_16x16x128_f8f6f4 v[74:77], v[10:17], v[222:229], 0, v180, v180 op_sel_hi:[0,0,0]
	v_mfma_scale_f32_16x16x128_f8f6f4 v[70:73], v[2:9], v[236:243], 0, v180, v180 op_sel_hi:[0,0,0]
	v_mfma_scale_f32_16x16x128_f8f6f4 v[66:69], v[10:17], v[236:243], 0, v180, v180 op_sel_hi:[0,0,0]
	v_mfma_scale_f32_16x16x128_f8f6f4 v[46:49], v[2:9], v[244:251], 0, v180, v180 op_sel_hi:[0,0,0]
	v_mfma_scale_f32_16x16x128_f8f6f4 v[42:45], v[10:17], v[244:251], 0, v180, v180 op_sel_hi:[0,0,0]
	v_mfma_scale_f32_16x16x128_f8f6f4 v[38:41], v[2:9], v[212:219], 0, v180, v180 op_sel_hi:[0,0,0]
	v_mfma_scale_f32_16x16x128_f8f6f4 v[34:37], v[10:17], v[212:219], 0, v180, v180 op_sel_hi:[0,0,0]
	s_setprio 0
	s_barrier
	ds_read_b128 v[2:5], v186
	ds_read_b128 v[10:13], v187
	ds_read_b128 v[6:9], v202
	ds_read_b128 v[14:17], v203
	ds_read_b128 v[18:21], v188
	ds_read_b128 v[26:29], v189
	ds_read_b128 v[22:25], v206
	ds_read_b128 v[30:33], v207
	s_add_u32 s18, s24, 0x20000
	s_addc_u32 s19, s25, 0
	s_mov_b32 m0, s44
	v_lshl_add_u64 v[252:253], s[18:19], 0, v[164:165]
	ds_read_b128 v[212:215], v234 offset:32768
	ds_read_b128 v[222:225], v234 offset:34816
	ds_read_b128 v[216:219], v208
	ds_read_b128 v[226:229], v209
	ds_read_b128 v[236:239], v234 offset:36864
	ds_read_b128 v[244:247], v234 offset:38912
	ds_read_b128 v[240:243], v210
	ds_read_b128 v[248:251], v211
	global_load_lds_dwordx4 v[252:253], off
	v_lshl_add_u64 v[252:253], s[18:19], 0, v[166:167]
	s_mov_b32 m0, s45
	s_nop 0
	global_load_lds_dwordx4 v[252:253], off
	s_waitcnt vmcnt(8)
	s_waitcnt lgkmcnt(0)
	s_barrier
	s_setprio 1
	s_waitcnt lgkmcnt(0)
	v_mfma_scale_f32_16x16x128_f8f6f4 v[158:161], v[2:9], v[212:219], v[158:161], v180, v180 op_sel_hi:[0,0,0]
	v_mfma_scale_f32_16x16x128_f8f6f4 v[154:157], v[10:17], v[212:219], v[154:157], v180, v180 op_sel_hi:[0,0,0]
	v_mfma_scale_f32_16x16x128_f8f6f4 v[150:153], v[2:9], v[222:229], v[150:153], v180, v180 op_sel_hi:[0,0,0]
	v_mfma_scale_f32_16x16x128_f8f6f4 v[146:149], v[10:17], v[222:229], v[146:149], v180, v180 op_sel_hi:[0,0,0]
	v_mfma_scale_f32_16x16x128_f8f6f4 v[126:129], v[2:9], v[236:243], v[126:129], v180, v180 op_sel_hi:[0,0,0]
	v_mfma_scale_f32_16x16x128_f8f6f4 v[122:125], v[10:17], v[236:243], v[122:125], v180, v180 op_sel_hi:[0,0,0]
	v_mfma_scale_f32_16x16x128_f8f6f4 v[118:121], v[2:9], v[244:251], v[118:121], v180, v180 op_sel_hi:[0,0,0]
	v_mfma_scale_f32_16x16x128_f8f6f4 v[114:117], v[10:17], v[244:251], v[114:117], v180, v180 op_sel_hi:[0,0,0]
	s_setprio 0
	s_setprio 1
	v_mfma_scale_f32_16x16x128_f8f6f4 v[142:145], v[18:25], v[212:219], v[142:145], v180, v180 op_sel_hi:[0,0,0]
	v_mfma_scale_f32_16x16x128_f8f6f4 v[138:141], v[26:33], v[212:219], v[138:141], v180, v180 op_sel_hi:[0,0,0]
	v_mfma_scale_f32_16x16x128_f8f6f4 v[134:137], v[18:25], v[222:229], v[134:137], v180, v180 op_sel_hi:[0,0,0]
	v_mfma_scale_f32_16x16x128_f8f6f4 v[130:133], v[26:33], v[222:229], v[130:133], v180, v180 op_sel_hi:[0,0,0]
	v_mfma_scale_f32_16x16x128_f8f6f4 v[110:113], v[18:25], v[236:243], v[110:113], v180, v180 op_sel_hi:[0,0,0]
	v_mfma_scale_f32_16x16x128_f8f6f4 v[106:109], v[26:33], v[236:243], v[106:109], v180, v180 op_sel_hi:[0,0,0]
	v_mfma_scale_f32_16x16x128_f8f6f4 v[102:105], v[18:25], v[244:251], v[102:105], v180, v180 op_sel_hi:[0,0,0]
	v_mfma_scale_f32_16x16x128_f8f6f4 v[98:101], v[26:33], v[244:251], v[98:101], v180, v180 op_sel_hi:[0,0,0]
	s_setprio 0
	s_barrier
	s_mov_b32 m0, s46
	v_lshl_add_u64 v[172:173], v[172:173], 0, s[78:79]
	s_add_u32 s18, s22, 0x20080
	ds_read_b128 v[212:215], v234 offset:49152
	ds_read_b128 v[222:225], v234 offset:51200
	ds_read_b128 v[216:219], v230
	ds_read_b128 v[226:229], v231
	ds_read_b128 v[236:239], v234 offset:53248
	ds_read_b128 v[244:247], v234 offset:55296
	ds_read_b128 v[240:243], v232
	ds_read_b128 v[248:251], v233
	global_load_lds_dwordx4 v[172:173], off
	v_lshl_add_u64 v[172:173], v[174:175], 0, s[78:79]
	s_mov_b32 m0, s48
	s_addc_u32 s19, s23, 0
	global_load_lds_dwordx4 v[172:173], off
	v_lshl_add_u64 v[172:173], s[18:19], 0, v[0:1]
	s_mov_b32 m0, s53
	s_nop 0
	global_load_lds_dwordx4 v[172:173], off
	v_lshl_add_u64 v[172:173], s[18:19], 0, v[162:163]
	s_mov_b32 m0, s54
	s_nop 0
	global_load_lds_dwordx4 v[172:173], off
	v_lshl_add_u64 v[172:173], v[176:177], 0, s[78:79]
	s_mov_b32 m0, s51
	s_nop 0
	global_load_lds_dwordx4 v[172:173], off
	v_lshl_add_u64 v[172:173], v[178:179], 0, s[78:79]
	s_mov_b32 m0, s52
	s_nop 0
	global_load_lds_dwordx4 v[172:173], off
	s_waitcnt vmcnt(8)
	s_waitcnt lgkmcnt(0)
	s_barrier
	s_setprio 1
	s_waitcnt lgkmcnt(0)
	v_mfma_scale_f32_16x16x128_f8f6f4 v[94:97], v[2:9], v[212:219], v[94:97], v180, v180 op_sel_hi:[0,0,0]
	v_mfma_scale_f32_16x16x128_f8f6f4 v[90:93], v[10:17], v[212:219], v[90:93], v180, v180 op_sel_hi:[0,0,0]
	v_mfma_scale_f32_16x16x128_f8f6f4 v[86:89], v[2:9], v[222:229], v[86:89], v180, v180 op_sel_hi:[0,0,0]
	v_mfma_scale_f32_16x16x128_f8f6f4 v[82:85], v[10:17], v[222:229], v[82:85], v180, v180 op_sel_hi:[0,0,0]
	v_mfma_scale_f32_16x16x128_f8f6f4 v[62:65], v[2:9], v[236:243], v[62:65], v180, v180 op_sel_hi:[0,0,0]
	v_mfma_scale_f32_16x16x128_f8f6f4 v[58:61], v[10:17], v[236:243], v[58:61], v180, v180 op_sel_hi:[0,0,0]
	v_mfma_scale_f32_16x16x128_f8f6f4 v[54:57], v[2:9], v[244:251], v[54:57], v180, v180 op_sel_hi:[0,0,0]
	v_mfma_scale_f32_16x16x128_f8f6f4 v[50:53], v[10:17], v[244:251], v[50:53], v180, v180 op_sel_hi:[0,0,0]
	s_setprio 0
	s_setprio 1
	v_mfma_scale_f32_16x16x128_f8f6f4 v[78:81], v[18:25], v[212:219], v[78:81], v180, v180 op_sel_hi:[0,0,0]
	v_mfma_scale_f32_16x16x128_f8f6f4 v[74:77], v[26:33], v[212:219], v[74:77], v180, v180 op_sel_hi:[0,0,0]
	v_mfma_scale_f32_16x16x128_f8f6f4 v[70:73], v[18:25], v[222:229], v[70:73], v180, v180 op_sel_hi:[0,0,0]
	v_mfma_scale_f32_16x16x128_f8f6f4 v[66:69], v[26:33], v[222:229], v[66:69], v180, v180 op_sel_hi:[0,0,0]
	v_mfma_scale_f32_16x16x128_f8f6f4 v[46:49], v[18:25], v[236:243], v[46:49], v180, v180 op_sel_hi:[0,0,0]
	v_mfma_scale_f32_16x16x128_f8f6f4 v[42:45], v[26:33], v[236:243], v[42:45], v180, v180 op_sel_hi:[0,0,0]
	v_mfma_scale_f32_16x16x128_f8f6f4 v[38:41], v[18:25], v[244:251], v[38:41], v180, v180 op_sel_hi:[0,0,0]
	v_mfma_scale_f32_16x16x128_f8f6f4 v[34:37], v[26:33], v[244:251], v[34:37], v180, v180 op_sel_hi:[0,0,0]
	s_setprio 0
	s_barrier
	s_add_i32 s68, s68, 2
	s_add_u32 s13, s13, 0x100
	s_addc_u32 s49, s49, 0
	s_cmp_gt_u32 s68, 5
	s_mov_b64 s[18:19], s[20:21]
